# v9 with 112 converter workgroups
# baseline (speedup 1.0000x reference)
.LBB0_226:
	s_cmp_lt_i32 s28, 3
	s_cselect_b64 s[0:1], -1, 0
	s_cmp_gt_i32 s29, 2
	s_cselect_b64 s[6:7], -1, 0
	s_and_b64 s[0:1], s[0:1], s[6:7]
	s_andn2_b64 vcc, exec, s[0:1]
	s_cbranch_vccnz .LBB0_398
	s_cmpk_lg_i32 s33, 0x100
	s_cselect_b32 s3, s33, 0x70
	s_sub_i32 s6, s33, s3
	s_cmp_lt_i32 s2, s6
	s_cselect_b64 s[0:1], -1, 0
	s_sub_i32 s30, s2, s6
	s_cmpk_gt_i32 s30, 0x2fff
	s_cselect_b64 s[6:7], -1, 0
	s_or_b64 s[0:1], s[0:1], s[6:7]
	v_lshrrev_b32_e32 v82, 5, v0
	v_lshlrev_b32_e32 v80, 4, v0
	v_lshrrev_b32_e32 v1, 7, v0
	v_lshrrev_b32_e32 v81, 3, v0
	s_and_b64 vcc, exec, s[0:1]
	s_cbranch_vccnz .LBB0_237
	v_readlane_b32 s6, v252, 0
	v_readlane_b32 s7, v252, 1
	v_readfirstlane_b32 s34, v0
	s_nop 4
	s_sub_u32 s6, s6, 0xe8
	s_subb_u32 s7, s7, 0
	s_load_dwordx2 s[8:9], s[6:7], 0xa8
	s_load_dwordx2 s[10:11], s[6:7], 0xb8
	s_lshr_b32 s34, s34, 6
	s_add_u32 s12, s26, 0x5800000
	s_addc_u32 s13, s27, 0
	s_add_u32 s14, s26, 0x25800000
	s_addc_u32 s15, s27, 0
	s_mov_b32 s35, 0xc3e00000
	v_mov_b32_e32 v160, 0x43e00000
	s_mov_b32 s31, 112
	s_sub_u32 s0, 0x2fff, s30
	s_mul_hi_u32 s41, s0, 0x2492493
	s_add_u32 s41, s41, 1
	v_and_b32_e32 v77, 63, v0
	v_and_b32_e32 v66, 31, v77
	v_lshlrev_b32_e32 v66, 4, v66
	v_lshrrev_b32_e32 v67, 5, v77
	v_lshlrev_b32_e32 v68, 4, v77
	v_lshl_add_u32 v69, v67, 9, v66
	s_lshr_b32 s0, s34, 1
	v_and_b32_e32 v78, 3, v77
	v_xor_b32_e32 v78, s0, v78
	v_and_b32_e32 v71, 4, v77
	v_or_b32_e32 v78, v78, v71
	v_lshlrev_b32_e32 v78, 4, v78
	s_and_b32 s0, s34, 1
	s_lshl_b32 s0, s0, 3
	v_lshl_or_b32 v71, v77, 9, s0
	v_or_b32_e32 v71, v71, v78
	v_xor_b32_e32 v72, 64, v71
	v_add_u32_e32 v73, 0x8000, v71
	v_add_u32_e32 v74, 0x8000, v72
	s_lshl_b32 s0, s34, 1
	v_add_u32_e32 v78, s0, v67
	v_xor_b32_e32 v78, v78, v77
	v_and_b32_e32 v78, 7, v78
	v_lshlrev_b32_e32 v78, 4, v78
	v_lshrrev_b32_e32 v75, 3, v77
	s_lshl_b32 s0, s34, 3
	v_add_u32_e32 v75, s0, v75
	v_and_b32_e32 v76, 7, v77
	v_lshlrev_b32_e32 v76, 4, v76
	v_lshl_add_u32 v76, v75, 11, v76
	v_lshl_add_u32 v75, v75, 7, v78
	s_waitcnt lgkmcnt(0)
	s_min_u32 s0, s30, 0x2fff
	s_add_u32 s30, s30, s31
	s_cmp_lt_u32 s0, 0x2000
	s_cbranch_scc0 .Lcv_w2_1
	s_lshr_b32 s1, s0, 8
	s_bfe_u32 s3, s0, 0x40004
	s_bfe_u32 s7, s0, 0x30001
	s_and_b32 s0, s0, 1
	s_lshl_b32 s6, s1, 25
	s_lshl_b32 s49, s3, 21
	s_add_u32 s6, s6, s49
	s_lshl_b32 s49, s34, 17
	s_add_u32 s6, s6, s49
	s_lshl_b32 s49, s0, 13
	s_add_u32 s6, s6, s49
	s_lshl_b32 s49, s7, 10
	s_add_u32 s6, s6, s49
	s_add_u32 s62, s8, s6
	s_addc_u32 s63, s9, 0
	s_lshl_b32 s6, s1, 23
	s_lshl_b32 s49, s7, 20
	s_add_u32 s6, s6, s49
	s_lshl_b32 s49, s0, 18
	s_add_u32 s6, s6, s49
	s_lshl_b32 s49, s3, 7
	s_add_u32 s6, s6, s49
	s_add_u32 s52, s12, s6
	s_addc_u32 s53, s13, 0
	s_mov_b32 s70, 0x4000
	s_mov_b32 s71, 0xe4000
	s_mov_b32 s86, 0x60000
	v_mov_b32_e32 v70, v68
	s_branch .Lcv_dec_done_1
